# gate/up epilogues: each activation store's address is one v_lshl_add_u32 + SALU-summed base pair instead of v_lshlrev_b64 + 3 v_lshl_add_u64 (both layers, 8 stores)
# speedup vs baseline: 1.0030x; 1.0030x over previous
.LBB0_1546:
	s_mov_b32 s73, 0xc2700000
	v_mov_b32_e32 v184, 0x41898193
	v_lshlrev_b32_e32 v150, 16, v86
	v_and_b32_e32 v151, 0xffff0000, v86
	v_mul_f32_e32 v158, 0x3d800000, v177
	v_pk_fma_f32 v[130:131], v[158:159], v[130:131], v[150:151] op_sel_hi:[0,1,1]
	v_med3_f32 v130, v130, s73, v184
	v_med3_f32 v131, v131, s73, v184
	v_exp_f32_e64 v178, -v130
	v_exp_f32_e64 v179, -v131
	v_lshlrev_b32_e32 v156, 16, v87
	v_and_b32_e32 v157, 0xffff0000, v87
	v_lshlrev_b32_e32 v152, 16, v82
	v_pk_add_f32 v[178:179], v[178:179], 1.0 op_sel_hi:[1,0]
	v_and_b32_e32 v153, 0xffff0000, v82
	v_lshlrev_b32_e32 v154, 16, v83
	v_and_b32_e32 v155, 0xffff0000, v83
	v_pk_fma_f32 v[132:133], v[158:159], v[132:133], v[156:157] op_sel_hi:[0,1,1]
	v_pk_fma_f32 v[134:135], v[158:159], v[134:135], v[152:153] op_sel_hi:[0,1,1]
	v_pk_fma_f32 v[136:137], v[158:159], v[136:137], v[154:155] op_sel_hi:[0,1,1]
	v_med3_f32 v134, v134, s70, v167
	v_med3_f32 v135, v135, s70, v167
	v_med3_f32 v132, v132, s73, v184
	v_med3_f32 v133, v133, s73, v184
	v_pk_mul_f32 v[130:131], v[130:131], v[134:135]
	v_med3_f32 v134, v136, s70, v167
	v_med3_f32 v135, v137, s70, v167
	v_exp_f32_e64 v136, -v132
	v_exp_f32_e64 v137, -v133
	v_lshlrev_b32_e32 v86, 16, v88
	v_and_b32_e32 v87, 0xffff0000, v88
	v_pk_fma_f32 v[122:123], v[158:159], v[122:123], v[86:87] op_sel_hi:[0,1,1]
	v_pk_add_f32 v[136:137], v[136:137], 1.0 op_sel_hi:[1,0]
	v_med3_f32 v122, v122, s73, v184
	v_pk_mul_f32 v[180:181], v[178:179], v[136:137]
	v_rcp_f32_e32 v180, v180
	v_rcp_f32_e32 v181, v181
	s_nop 0
	v_pk_mul_f32 v[182:183], v[180:181], v[136:137]
	v_pk_mul_f32 v[136:137], v[180:181], v[178:179]
	v_pk_mul_f32 v[130:131], v[130:131], v[182:183]
	v_med3_f32 v123, v123, s73, v184
	v_lshlrev_b32_e32 v88, 16, v89
	v_and_b32_e32 v89, 0xffff0000, v89
	v_pk_mul_f32 v[132:133], v[132:133], v[136:137]
	v_lshlrev_b32_e32 v82, 16, v84
	v_pk_mul_f32 v[132:133], v[132:133], v[134:135]
	v_exp_f32_e64 v134, -v122
	v_exp_f32_e64 v135, -v123
	v_and_b32_e32 v83, 0xffff0000, v84
	v_lshlrev_b32_e32 v84, 16, v85
	v_and_b32_e32 v85, 0xffff0000, v85
	v_pk_add_f32 v[134:135], v[134:135], 1.0 op_sel_hi:[1,0]
	v_pk_fma_f32 v[124:125], v[158:159], v[124:125], v[88:89] op_sel_hi:[0,1,1]
	v_pk_fma_f32 v[126:127], v[158:159], v[126:127], v[82:83] op_sel_hi:[0,1,1]
	v_pk_fma_f32 v[128:129], v[158:159], v[128:129], v[84:85] op_sel_hi:[0,1,1]
	v_med3_f32 v126, v126, s70, v167
	v_med3_f32 v127, v127, s70, v167
	v_med3_f32 v124, v124, s73, v184
	v_med3_f32 v125, v125, s73, v184
	v_pk_mul_f32 v[122:123], v[122:123], v[126:127]
	v_med3_f32 v126, v128, s70, v167
	v_med3_f32 v127, v129, s70, v167
	v_exp_f32_e64 v128, -v124
	v_exp_f32_e64 v129, -v125
	v_mov_b32_e32 v142, v0
	s_and_b64 vcc, exec, s[6:7]
	v_pk_add_f32 v[128:129], v[128:129], 1.0 op_sel_hi:[1,0]
	v_readfirstlane_b32 s69, v142
	v_pk_mul_f32 v[180:181], v[134:135], v[128:129]
	v_rcp_f32_e32 v180, v180
	v_rcp_f32_e32 v181, v181
	s_nop 0
	v_pk_mul_f32 v[182:183], v[180:181], v[128:129]
	v_pk_mul_f32 v[128:129], v[180:181], v[134:135]
	v_pk_mul_f32 v[122:123], v[122:123], v[182:183]
	s_ashr_i32 s8, s69, 6
	s_mul_i32 s9, s8, 0xb00
	s_add_i32 s71, s9, 0
	v_pk_mul_f32 v[124:125], v[124:125], v[128:129]
	v_and_b32_e32 v147, 15, v142
	v_pk_mul_f32 v[124:125], v[124:125], v[126:127]
	v_mov_b32_e32 v126, 0
	v_mov_b32_e32 v127, 0
	v_cvt_pk_fp8_f32 v126, v130, v131
	v_cvt_pk_fp8_f32 v127, v122, v123
	v_lshrrev_b32_e32 v123, 1, v142
	s_add_i32 s71, s71, 0x20000
	v_cvt_pk_fp8_f32 v126, v132, v133 op_sel:[0,0,1]
	v_cvt_pk_fp8_f32 v127, v124, v125 op_sel:[0,0,1]
	v_mul_f32_e32 v124, 0x3d800000, v176
	v_mul_u32_u24_e32 v122, 48, v147
	v_and_b32_e32 v123, 24, v123
	v_pk_fma_f32 v[114:115], v[124:125], v[114:115], v[150:151] op_sel_hi:[0,1,1]
	v_add3_u32 v122, s71, v122, v123
	v_med3_f32 v114, v114, s73, v184
	v_med3_f32 v115, v115, s73, v184
	ds_write_b64 v122, v[126:127]
	v_exp_f32_e64 v126, -v114
	v_exp_f32_e64 v127, -v115
	v_pk_fma_f32 v[116:117], v[124:125], v[116:117], v[156:157] op_sel_hi:[0,1,1]
	v_pk_fma_f32 v[118:119], v[124:125], v[118:119], v[152:153] op_sel_hi:[0,1,1]
	v_pk_fma_f32 v[120:121], v[124:125], v[120:121], v[154:155] op_sel_hi:[0,1,1]
	v_pk_add_f32 v[126:127], v[126:127], 1.0 op_sel_hi:[1,0]
	v_med3_f32 v118, v118, s70, v167
	v_med3_f32 v119, v119, s70, v167
	v_med3_f32 v116, v116, s73, v184
	v_med3_f32 v117, v117, s73, v184
	v_pk_fma_f32 v[106:107], v[124:125], v[106:107], v[86:87] op_sel_hi:[0,1,1]
	v_pk_mul_f32 v[114:115], v[114:115], v[118:119]
	v_med3_f32 v118, v120, s70, v167
	v_med3_f32 v119, v121, s70, v167
	v_exp_f32_e64 v120, -v116
	v_exp_f32_e64 v121, -v117
	v_med3_f32 v106, v106, s73, v184
	v_med3_f32 v107, v107, s73, v184
	v_pk_fma_f32 v[108:109], v[124:125], v[108:109], v[88:89] op_sel_hi:[0,1,1]
	v_pk_add_f32 v[120:121], v[120:121], 1.0 op_sel_hi:[1,0]
	v_pk_fma_f32 v[110:111], v[124:125], v[110:111], v[82:83] op_sel_hi:[0,1,1]
	v_pk_mul_f32 v[180:181], v[126:127], v[120:121]
	v_rcp_f32_e32 v180, v180
	v_rcp_f32_e32 v181, v181
	s_nop 0
	v_pk_mul_f32 v[182:183], v[180:181], v[120:121]
	v_pk_mul_f32 v[120:121], v[180:181], v[126:127]
	v_pk_mul_f32 v[114:115], v[114:115], v[182:183]
	v_pk_fma_f32 v[112:113], v[124:125], v[112:113], v[84:85] op_sel_hi:[0,1,1]
	v_med3_f32 v110, v110, s70, v167
	v_med3_f32 v111, v111, s70, v167
	v_pk_mul_f32 v[116:117], v[116:117], v[120:121]
	v_med3_f32 v108, v108, s73, v184
	v_pk_mul_f32 v[116:117], v[116:117], v[118:119]
	v_exp_f32_e64 v118, -v106
	v_exp_f32_e64 v119, -v107
	v_med3_f32 v109, v109, s73, v184
	s_ashr_i32 s69, s69, 2
	s_andn2_b32 s69, s69, 63
	v_pk_add_f32 v[118:119], v[118:119], 1.0 op_sel_hi:[1,0]
	s_lshl_b32 s8, s8, 5
	s_lshl_b32 s9, s80, 7
	s_and_b32 s8, s8, 0x60
	s_or_b32 s8, s8, s9
	s_ashr_i32 s9, s8, 31
	v_pk_mul_f32 v[106:107], v[106:107], v[110:111]
	v_med3_f32 v110, v112, s70, v167
	v_med3_f32 v111, v113, s70, v167
	v_exp_f32_e64 v112, -v108
	v_exp_f32_e64 v113, -v109
	s_nop 0
	v_pk_add_f32 v[112:113], v[112:113], 1.0 op_sel_hi:[1,0]
	s_nop 0
	v_pk_mul_f32 v[180:181], v[118:119], v[112:113]
	v_rcp_f32_e32 v180, v180
	v_rcp_f32_e32 v181, v181
	s_nop 0
	v_pk_mul_f32 v[182:183], v[180:181], v[112:113]
	v_pk_mul_f32 v[112:113], v[180:181], v[118:119]
	v_pk_mul_f32 v[106:107], v[106:107], v[182:183]
	s_nop 0
	v_pk_mul_f32 v[108:109], v[108:109], v[112:113]
	s_nop 0
	v_pk_mul_f32 v[108:109], v[108:109], v[110:111]
	v_mov_b32_e32 v110, 0
	v_mov_b32_e32 v111, 0
	v_cvt_pk_fp8_f32 v110, v114, v115
	v_cvt_pk_fp8_f32 v111, v106, v107
	v_bfe_u32 v106, v142, 1, 5
	v_mul_u32_u24_e32 v107, 48, v106
	v_cvt_pk_fp8_f32 v110, v116, v117 op_sel:[0,0,1]
	v_cvt_pk_fp8_f32 v111, v108, v109 op_sel:[0,0,1]
	v_lshlrev_b32_e32 v108, 4, v142
	v_and_b32_e32 v142, 16, v108
	v_lshl_or_b32 v106, s78, 8, v106
	ds_write_b64 v122, v[110:111] offset:768
	v_add3_u32 v108, s71, v107, v142
	v_add_u32_e32 v106, s69, v106
	ds_read_b128 v[110:113], v108
	v_ashrrev_i32_e32 v107, 31, v106
	v_lshl_add_u32 v114, v106, 10, v142
	s_add_u32 s86, s16, s8
	s_addc_u32 s87, s17, s9
	s_waitcnt lgkmcnt(0)
	global_store_dwordx4 v114, v[110:113], s[86:87]
	s_nop 1
	v_mul_f32_e32 v110, 0x3d800000, v175
	v_pk_fma_f32 v[98:99], v[110:111], v[98:99], v[150:151] op_sel_hi:[0,1,1]
	v_med3_f32 v98, v98, s73, v184
	v_med3_f32 v99, v99, s73, v184
	v_exp_f32_e64 v112, -v98
	v_exp_f32_e64 v113, -v99
	v_pk_fma_f32 v[100:101], v[110:111], v[100:101], v[156:157] op_sel_hi:[0,1,1]
	v_pk_fma_f32 v[102:103], v[110:111], v[102:103], v[152:153] op_sel_hi:[0,1,1]
	v_pk_fma_f32 v[104:105], v[110:111], v[104:105], v[154:155] op_sel_hi:[0,1,1]
	v_pk_add_f32 v[112:113], v[112:113], 1.0 op_sel_hi:[1,0]
	v_med3_f32 v102, v102, s70, v167
	v_med3_f32 v103, v103, s70, v167
	v_med3_f32 v100, v100, s73, v184
	v_med3_f32 v101, v101, s73, v184
	v_pk_fma_f32 v[90:91], v[110:111], v[90:91], v[86:87] op_sel_hi:[0,1,1]
	v_pk_mul_f32 v[98:99], v[98:99], v[102:103]
	v_med3_f32 v102, v104, s70, v167
	v_med3_f32 v103, v105, s70, v167
	v_exp_f32_e64 v104, -v100
	v_exp_f32_e64 v105, -v101
	v_med3_f32 v90, v90, s73, v184
	v_med3_f32 v91, v91, s73, v184
	v_pk_fma_f32 v[92:93], v[110:111], v[92:93], v[88:89] op_sel_hi:[0,1,1]
	v_pk_add_f32 v[104:105], v[104:105], 1.0 op_sel_hi:[1,0]
	v_pk_fma_f32 v[94:95], v[110:111], v[94:95], v[82:83] op_sel_hi:[0,1,1]
	v_pk_mul_f32 v[180:181], v[112:113], v[104:105]
	v_rcp_f32_e32 v180, v180
	v_rcp_f32_e32 v181, v181
	s_nop 0
	v_pk_mul_f32 v[182:183], v[180:181], v[104:105]
	v_pk_mul_f32 v[104:105], v[180:181], v[112:113]
	v_pk_mul_f32 v[98:99], v[98:99], v[182:183]
	v_pk_fma_f32 v[96:97], v[110:111], v[96:97], v[84:85] op_sel_hi:[0,1,1]
	v_med3_f32 v94, v94, s70, v167
	v_med3_f32 v95, v95, s70, v167
	v_pk_mul_f32 v[100:101], v[100:101], v[104:105]
	v_med3_f32 v92, v92, s73, v184
	v_pk_mul_f32 v[100:101], v[100:101], v[102:103]
	v_exp_f32_e64 v102, -v90
	v_exp_f32_e64 v103, -v91
	v_med3_f32 v93, v93, s73, v184
	v_pk_add_f32 v[102:103], v[102:103], 1.0 op_sel_hi:[1,0]
	s_nop 0
	s_nop 0
	s_nop 0
	v_pk_mul_f32 v[90:91], v[90:91], v[94:95]
	v_med3_f32 v94, v96, s70, v167
	v_med3_f32 v95, v97, s70, v167
	v_exp_f32_e64 v96, -v92
	v_exp_f32_e64 v97, -v93
	s_nop 0
	v_pk_add_f32 v[96:97], v[96:97], 1.0 op_sel_hi:[1,0]
	s_nop 0
	v_pk_mul_f32 v[180:181], v[102:103], v[96:97]
	v_rcp_f32_e32 v180, v180
	v_rcp_f32_e32 v181, v181
	s_nop 0
	v_pk_mul_f32 v[182:183], v[180:181], v[96:97]
	v_pk_mul_f32 v[96:97], v[180:181], v[102:103]
	v_pk_mul_f32 v[90:91], v[90:91], v[182:183]
	s_nop 0
	v_pk_mul_f32 v[92:93], v[92:93], v[96:97]
	s_nop 0
	v_pk_mul_f32 v[92:93], v[92:93], v[94:95]
	v_mov_b32_e32 v95, v143
	v_cvt_pk_fp8_f32 v95, v90, v91
	v_mul_f32_e32 v90, 0x3d800000, v174
	v_pk_fma_f32 v[74:75], v[90:91], v[74:75], v[150:151] op_sel_hi:[0,1,1]
	v_med3_f32 v74, v74, s73, v184
	v_med3_f32 v75, v75, s73, v184
	v_cvt_pk_fp8_f32 v95, v92, v93 op_sel:[0,0,1]
	v_exp_f32_e64 v92, -v74
	v_exp_f32_e64 v93, -v75
	v_pk_fma_f32 v[76:77], v[90:91], v[76:77], v[156:157] op_sel_hi:[0,1,1]
	v_pk_fma_f32 v[78:79], v[90:91], v[78:79], v[152:153] op_sel_hi:[0,1,1]
	v_pk_fma_f32 v[80:81], v[90:91], v[80:81], v[154:155] op_sel_hi:[0,1,1]
	v_pk_add_f32 v[92:93], v[92:93], 1.0 op_sel_hi:[1,0]
	v_med3_f32 v78, v78, s70, v167
	v_med3_f32 v79, v79, s70, v167
	v_med3_f32 v76, v76, s73, v184
	v_med3_f32 v77, v77, s73, v184
	v_pk_fma_f32 v[66:67], v[90:91], v[66:67], v[86:87] op_sel_hi:[0,1,1]
	v_pk_mul_f32 v[74:75], v[74:75], v[78:79]
	v_med3_f32 v78, v80, s70, v167
	v_med3_f32 v79, v81, s70, v167
	v_exp_f32_e64 v80, -v76
	v_exp_f32_e64 v81, -v77
	v_med3_f32 v66, v66, s73, v184
	v_med3_f32 v67, v67, s73, v184
	v_pk_fma_f32 v[68:69], v[90:91], v[68:69], v[88:89] op_sel_hi:[0,1,1]
	v_pk_add_f32 v[80:81], v[80:81], 1.0 op_sel_hi:[1,0]
	v_pk_fma_f32 v[70:71], v[90:91], v[70:71], v[82:83] op_sel_hi:[0,1,1]
	v_pk_mul_f32 v[180:181], v[92:93], v[80:81]
	v_rcp_f32_e32 v180, v180
	v_rcp_f32_e32 v181, v181
	s_nop 0
	v_pk_mul_f32 v[182:183], v[180:181], v[80:81]
	v_pk_mul_f32 v[80:81], v[180:181], v[92:93]
	v_pk_mul_f32 v[74:75], v[74:75], v[182:183]
	v_pk_fma_f32 v[72:73], v[90:91], v[72:73], v[84:85] op_sel_hi:[0,1,1]
	v_med3_f32 v70, v70, s70, v167
	v_med3_f32 v71, v71, s70, v167
	v_pk_mul_f32 v[76:77], v[76:77], v[80:81]
	v_med3_f32 v68, v68, s73, v184
	v_pk_mul_f32 v[76:77], v[76:77], v[78:79]
	v_exp_f32_e64 v78, -v66
	v_exp_f32_e64 v79, -v67
	v_med3_f32 v69, v69, s73, v184
	v_mov_b32_e32 v94, v143
	v_cvt_pk_fp8_f32 v94, v98, v99
	v_pk_add_f32 v[78:79], v[78:79], 1.0 op_sel_hi:[1,0]
	v_cvt_pk_fp8_f32 v94, v100, v101 op_sel:[0,0,1]
	ds_write_b64 v122, v[94:95]
	s_nop 0
	v_pk_mul_f32 v[66:67], v[66:67], v[70:71]
	v_med3_f32 v70, v72, s70, v167
	v_med3_f32 v71, v73, s70, v167
	v_exp_f32_e64 v72, -v68
	v_exp_f32_e64 v73, -v69
	s_nop 0
	v_pk_add_f32 v[72:73], v[72:73], 1.0 op_sel_hi:[1,0]
	s_nop 0
	v_pk_mul_f32 v[180:181], v[78:79], v[72:73]
	v_rcp_f32_e32 v180, v180
	v_rcp_f32_e32 v181, v181
	s_nop 0
	v_pk_mul_f32 v[182:183], v[180:181], v[72:73]
	v_pk_mul_f32 v[72:73], v[180:181], v[78:79]
	v_pk_mul_f32 v[66:67], v[66:67], v[182:183]
	s_nop 0
	v_pk_mul_f32 v[68:69], v[68:69], v[72:73]
	s_nop 0
	v_pk_mul_f32 v[68:69], v[68:69], v[70:71]
	v_mov_b32_e32 v70, v143
	v_mov_b32_e32 v71, v143
	v_cvt_pk_fp8_f32 v70, v74, v75
	v_cvt_pk_fp8_f32 v71, v66, v67
	v_cvt_pk_fp8_f32 v70, v76, v77 op_sel:[0,0,1]
	v_cvt_pk_fp8_f32 v71, v68, v69 op_sel:[0,0,1]
	ds_write_b64 v122, v[70:71] offset:768
	v_or_b32_e32 v70, 32, v106
	ds_read_b128 v[66:69], v108
	v_ashrrev_i32_e32 v71, 31, v70
	v_lshl_add_u32 v70, v70, 10, v142
	s_add_u32 s86, s16, s8
	s_addc_u32 s87, s17, s9
	s_waitcnt lgkmcnt(0)
	global_store_dwordx4 v70, v[66:69], s[86:87]
	s_nop 1
	v_mul_f32_e32 v66, 0x3d800000, v173
	v_pk_fma_f32 v[58:59], v[66:67], v[58:59], v[150:151] op_sel_hi:[0,1,1]
	v_med3_f32 v58, v58, s73, v184
	v_med3_f32 v59, v59, s73, v184
	v_exp_f32_e64 v68, -v58
	v_exp_f32_e64 v69, -v59
	v_pk_fma_f32 v[60:61], v[66:67], v[60:61], v[156:157] op_sel_hi:[0,1,1]
	v_pk_fma_f32 v[62:63], v[66:67], v[62:63], v[152:153] op_sel_hi:[0,1,1]
	v_pk_fma_f32 v[64:65], v[66:67], v[64:65], v[154:155] op_sel_hi:[0,1,1]
	v_pk_add_f32 v[68:69], v[68:69], 1.0 op_sel_hi:[1,0]
	v_med3_f32 v62, v62, s70, v167
	v_med3_f32 v63, v63, s70, v167
	v_med3_f32 v60, v60, s73, v184
	v_med3_f32 v61, v61, s73, v184
	v_pk_fma_f32 v[50:51], v[66:67], v[50:51], v[86:87] op_sel_hi:[0,1,1]
	v_pk_mul_f32 v[58:59], v[58:59], v[62:63]
	v_med3_f32 v62, v64, s70, v167
	v_med3_f32 v63, v65, s70, v167
	v_exp_f32_e64 v64, -v60
	v_exp_f32_e64 v65, -v61
	v_med3_f32 v50, v50, s73, v184
	v_med3_f32 v51, v51, s73, v184
	v_pk_fma_f32 v[52:53], v[66:67], v[52:53], v[88:89] op_sel_hi:[0,1,1]
	v_pk_add_f32 v[64:65], v[64:65], 1.0 op_sel_hi:[1,0]
	v_pk_fma_f32 v[54:55], v[66:67], v[54:55], v[82:83] op_sel_hi:[0,1,1]
	v_pk_mul_f32 v[180:181], v[68:69], v[64:65]
	v_rcp_f32_e32 v180, v180
	v_rcp_f32_e32 v181, v181
	s_nop 0
	v_pk_mul_f32 v[182:183], v[180:181], v[64:65]
	v_pk_mul_f32 v[64:65], v[180:181], v[68:69]
	v_pk_mul_f32 v[58:59], v[58:59], v[182:183]
	v_pk_fma_f32 v[56:57], v[66:67], v[56:57], v[84:85] op_sel_hi:[0,1,1]
	v_med3_f32 v54, v54, s70, v167
	v_med3_f32 v55, v55, s70, v167
	v_pk_mul_f32 v[60:61], v[60:61], v[64:65]
	v_med3_f32 v52, v52, s73, v184
	v_pk_mul_f32 v[60:61], v[60:61], v[62:63]
	v_exp_f32_e64 v62, -v50
	v_exp_f32_e64 v63, -v51
	v_med3_f32 v53, v53, s73, v184
	v_pk_add_f32 v[62:63], v[62:63], 1.0 op_sel_hi:[1,0]
	s_nop 0
	s_nop 0
	s_nop 0
	v_pk_mul_f32 v[50:51], v[50:51], v[54:55]
	v_med3_f32 v54, v56, s70, v167
	v_med3_f32 v55, v57, s70, v167
	v_exp_f32_e64 v56, -v52
	v_exp_f32_e64 v57, -v53
	s_nop 0
	v_pk_add_f32 v[56:57], v[56:57], 1.0 op_sel_hi:[1,0]
	s_nop 0
	v_pk_mul_f32 v[180:181], v[62:63], v[56:57]
	v_rcp_f32_e32 v180, v180
	v_rcp_f32_e32 v181, v181
	s_nop 0
	v_pk_mul_f32 v[182:183], v[180:181], v[56:57]
	v_pk_mul_f32 v[56:57], v[180:181], v[62:63]
	v_pk_mul_f32 v[50:51], v[50:51], v[182:183]
	s_nop 0
	v_pk_mul_f32 v[52:53], v[52:53], v[56:57]
	s_nop 0
	v_pk_mul_f32 v[52:53], v[52:53], v[54:55]
	v_mov_b32_e32 v55, v143
	v_cvt_pk_fp8_f32 v55, v50, v51
	v_mul_f32_e32 v50, 0x3d800000, v172
	v_pk_fma_f32 v[42:43], v[50:51], v[42:43], v[150:151] op_sel_hi:[0,1,1]
	v_med3_f32 v42, v42, s73, v184
	v_med3_f32 v43, v43, s73, v184
	v_cvt_pk_fp8_f32 v55, v52, v53 op_sel:[0,0,1]
	v_exp_f32_e64 v52, -v42
	v_exp_f32_e64 v53, -v43
	v_pk_fma_f32 v[44:45], v[50:51], v[44:45], v[156:157] op_sel_hi:[0,1,1]
	v_pk_fma_f32 v[46:47], v[50:51], v[46:47], v[152:153] op_sel_hi:[0,1,1]
	v_pk_fma_f32 v[48:49], v[50:51], v[48:49], v[154:155] op_sel_hi:[0,1,1]
	v_pk_add_f32 v[52:53], v[52:53], 1.0 op_sel_hi:[1,0]
	v_med3_f32 v46, v46, s70, v167
	v_med3_f32 v47, v47, s70, v167
	v_med3_f32 v44, v44, s73, v184
	v_med3_f32 v45, v45, s73, v184
	v_pk_fma_f32 v[34:35], v[50:51], v[34:35], v[86:87] op_sel_hi:[0,1,1]
	v_pk_mul_f32 v[42:43], v[42:43], v[46:47]
	v_med3_f32 v46, v48, s70, v167
	v_med3_f32 v47, v49, s70, v167
	v_exp_f32_e64 v48, -v44
	v_exp_f32_e64 v49, -v45
	v_med3_f32 v34, v34, s73, v184
	v_med3_f32 v35, v35, s73, v184
	v_pk_fma_f32 v[36:37], v[50:51], v[36:37], v[88:89] op_sel_hi:[0,1,1]
	v_pk_add_f32 v[48:49], v[48:49], 1.0 op_sel_hi:[1,0]
	v_pk_fma_f32 v[38:39], v[50:51], v[38:39], v[82:83] op_sel_hi:[0,1,1]
	v_pk_mul_f32 v[180:181], v[52:53], v[48:49]
	v_rcp_f32_e32 v180, v180
	v_rcp_f32_e32 v181, v181
	s_nop 0
	v_pk_mul_f32 v[182:183], v[180:181], v[48:49]
	v_pk_mul_f32 v[48:49], v[180:181], v[52:53]
	v_pk_mul_f32 v[42:43], v[42:43], v[182:183]
	v_pk_fma_f32 v[40:41], v[50:51], v[40:41], v[84:85] op_sel_hi:[0,1,1]
	v_med3_f32 v38, v38, s70, v167
	v_med3_f32 v39, v39, s70, v167
	v_pk_mul_f32 v[44:45], v[44:45], v[48:49]
	v_med3_f32 v36, v36, s73, v184
	v_pk_mul_f32 v[44:45], v[44:45], v[46:47]
	v_exp_f32_e64 v46, -v34
	v_exp_f32_e64 v47, -v35
	v_med3_f32 v37, v37, s73, v184
	v_mov_b32_e32 v54, v143
	v_cvt_pk_fp8_f32 v54, v58, v59
	v_pk_add_f32 v[46:47], v[46:47], 1.0 op_sel_hi:[1,0]
	v_cvt_pk_fp8_f32 v54, v60, v61 op_sel:[0,0,1]
	ds_write_b64 v122, v[54:55]
	s_nop 0
	v_pk_mul_f32 v[34:35], v[34:35], v[38:39]
	v_med3_f32 v38, v40, s70, v167
	v_med3_f32 v39, v41, s70, v167
	v_exp_f32_e64 v40, -v36
	v_exp_f32_e64 v41, -v37
	s_nop 0
	v_pk_add_f32 v[40:41], v[40:41], 1.0 op_sel_hi:[1,0]
	s_nop 0
	v_pk_mul_f32 v[180:181], v[46:47], v[40:41]
	v_rcp_f32_e32 v180, v180
	v_rcp_f32_e32 v181, v181
	s_nop 0
	v_pk_mul_f32 v[182:183], v[180:181], v[40:41]
	v_pk_mul_f32 v[40:41], v[180:181], v[46:47]
	v_pk_mul_f32 v[34:35], v[34:35], v[182:183]
	s_nop 0
	v_pk_mul_f32 v[36:37], v[36:37], v[40:41]
	s_nop 0
	v_pk_mul_f32 v[36:37], v[36:37], v[38:39]
	v_mov_b32_e32 v38, v143
	v_mov_b32_e32 v39, v143
	v_cvt_pk_fp8_f32 v38, v42, v43
	v_cvt_pk_fp8_f32 v39, v34, v35
	v_cvt_pk_fp8_f32 v38, v44, v45 op_sel:[0,0,1]
	v_cvt_pk_fp8_f32 v39, v36, v37 op_sel:[0,0,1]
	ds_write_b64 v122, v[38:39] offset:768
	v_add_u32_e32 v38, 0x80, v106
	ds_read_b128 v[34:37], v108
	v_ashrrev_i32_e32 v39, 31, v38
	v_lshl_add_u32 v38, v38, 10, v142
	s_add_u32 s86, s16, s8
	s_addc_u32 s87, s17, s9
	s_waitcnt lgkmcnt(0)
	global_store_dwordx4 v38, v[34:37], s[86:87]
	s_nop 1
	v_mul_f32_e32 v34, 0x3d800000, v171
	v_pk_fma_f32 v[26:27], v[34:35], v[26:27], v[150:151] op_sel_hi:[0,1,1]
	v_med3_f32 v26, v26, s73, v184
	v_med3_f32 v27, v27, s73, v184
	v_exp_f32_e64 v36, -v26
	v_exp_f32_e64 v37, -v27
	v_pk_fma_f32 v[28:29], v[34:35], v[28:29], v[156:157] op_sel_hi:[0,1,1]
	v_pk_fma_f32 v[30:31], v[34:35], v[30:31], v[152:153] op_sel_hi:[0,1,1]
	v_pk_fma_f32 v[32:33], v[34:35], v[32:33], v[154:155] op_sel_hi:[0,1,1]
	v_pk_add_f32 v[36:37], v[36:37], 1.0 op_sel_hi:[1,0]
	v_med3_f32 v30, v30, s70, v167
	v_med3_f32 v31, v31, s70, v167
	v_med3_f32 v28, v28, s73, v184
	v_med3_f32 v29, v29, s73, v184
	v_pk_fma_f32 v[18:19], v[34:35], v[18:19], v[86:87] op_sel_hi:[0,1,1]
	v_pk_mul_f32 v[26:27], v[26:27], v[30:31]
	v_med3_f32 v30, v32, s70, v167
	v_med3_f32 v31, v33, s70, v167
	v_exp_f32_e64 v32, -v28
	v_exp_f32_e64 v33, -v29
	v_med3_f32 v18, v18, s73, v184
	v_med3_f32 v19, v19, s73, v184
	v_pk_fma_f32 v[20:21], v[34:35], v[20:21], v[88:89] op_sel_hi:[0,1,1]
	v_pk_add_f32 v[32:33], v[32:33], 1.0 op_sel_hi:[1,0]
	v_pk_fma_f32 v[22:23], v[34:35], v[22:23], v[82:83] op_sel_hi:[0,1,1]
	v_pk_mul_f32 v[180:181], v[36:37], v[32:33]
	v_rcp_f32_e32 v180, v180
	v_rcp_f32_e32 v181, v181
	s_nop 0
	v_pk_mul_f32 v[182:183], v[180:181], v[32:33]
	v_pk_mul_f32 v[32:33], v[180:181], v[36:37]
	v_pk_mul_f32 v[26:27], v[26:27], v[182:183]
	v_pk_fma_f32 v[24:25], v[34:35], v[24:25], v[84:85] op_sel_hi:[0,1,1]
	v_med3_f32 v22, v22, s70, v167
	v_med3_f32 v23, v23, s70, v167
	v_pk_mul_f32 v[28:29], v[28:29], v[32:33]
	v_med3_f32 v20, v20, s73, v184
	v_pk_mul_f32 v[28:29], v[28:29], v[30:31]
	v_exp_f32_e64 v30, -v18
	v_exp_f32_e64 v31, -v19
	v_med3_f32 v21, v21, s73, v184
	v_pk_add_f32 v[30:31], v[30:31], 1.0 op_sel_hi:[1,0]
	s_nop 0
	s_nop 0
	s_nop 0
	v_pk_mul_f32 v[18:19], v[18:19], v[22:23]
	v_med3_f32 v22, v24, s70, v167
	v_med3_f32 v23, v25, s70, v167
	v_exp_f32_e64 v24, -v20
	v_exp_f32_e64 v25, -v21
	s_nop 0
	v_pk_add_f32 v[24:25], v[24:25], 1.0 op_sel_hi:[1,0]
	s_nop 0
	v_pk_mul_f32 v[180:181], v[30:31], v[24:25]
	v_rcp_f32_e32 v180, v180
	v_rcp_f32_e32 v181, v181
	s_nop 0
	v_pk_mul_f32 v[182:183], v[180:181], v[24:25]
	v_pk_mul_f32 v[24:25], v[180:181], v[30:31]
	v_pk_mul_f32 v[18:19], v[18:19], v[182:183]
	s_nop 0
	v_pk_mul_f32 v[20:21], v[20:21], v[24:25]
	s_nop 0
	v_pk_mul_f32 v[20:21], v[20:21], v[22:23]
	v_mov_b32_e32 v23, v143
	v_cvt_pk_fp8_f32 v23, v18, v19
	v_mul_f32_e32 v18, 0x3d800000, v168
	v_pk_fma_f32 v[10:11], v[18:19], v[10:11], v[150:151] op_sel_hi:[0,1,1]
	v_med3_f32 v10, v10, s73, v184
	v_med3_f32 v11, v11, s73, v184
	v_cvt_pk_fp8_f32 v23, v20, v21 op_sel:[0,0,1]
	v_exp_f32_e64 v20, -v10
	v_exp_f32_e64 v21, -v11
	v_pk_fma_f32 v[12:13], v[18:19], v[12:13], v[156:157] op_sel_hi:[0,1,1]
	v_pk_fma_f32 v[14:15], v[18:19], v[14:15], v[152:153] op_sel_hi:[0,1,1]
	v_pk_fma_f32 v[16:17], v[18:19], v[16:17], v[154:155] op_sel_hi:[0,1,1]
	v_pk_add_f32 v[20:21], v[20:21], 1.0 op_sel_hi:[1,0]
	v_med3_f32 v14, v14, s70, v167
	v_med3_f32 v15, v15, s70, v167
	v_med3_f32 v12, v12, s73, v184
	v_med3_f32 v13, v13, s73, v184
	v_pk_fma_f32 v[2:3], v[18:19], v[2:3], v[86:87] op_sel_hi:[0,1,1]
	v_pk_mul_f32 v[10:11], v[10:11], v[14:15]
	v_med3_f32 v14, v16, s70, v167
	v_med3_f32 v15, v17, s70, v167
	v_exp_f32_e64 v16, -v12
	v_exp_f32_e64 v17, -v13
	v_med3_f32 v2, v2, s73, v184
	v_med3_f32 v3, v3, s73, v184
	v_pk_fma_f32 v[4:5], v[18:19], v[4:5], v[88:89] op_sel_hi:[0,1,1]
	v_pk_add_f32 v[16:17], v[16:17], 1.0 op_sel_hi:[1,0]
	v_pk_fma_f32 v[6:7], v[18:19], v[6:7], v[82:83] op_sel_hi:[0,1,1]
	v_pk_mul_f32 v[180:181], v[20:21], v[16:17]
	v_rcp_f32_e32 v180, v180
	v_rcp_f32_e32 v181, v181
	s_nop 0
	v_pk_mul_f32 v[182:183], v[180:181], v[16:17]
	v_pk_mul_f32 v[16:17], v[180:181], v[20:21]
	v_pk_mul_f32 v[10:11], v[10:11], v[182:183]
	v_pk_fma_f32 v[8:9], v[18:19], v[8:9], v[84:85] op_sel_hi:[0,1,1]
	v_med3_f32 v6, v6, s70, v167
	v_med3_f32 v7, v7, s70, v167
	v_pk_mul_f32 v[12:13], v[12:13], v[16:17]
	v_med3_f32 v4, v4, s73, v184
	v_pk_mul_f32 v[12:13], v[12:13], v[14:15]
	v_exp_f32_e64 v14, -v2
	v_exp_f32_e64 v15, -v3
	v_med3_f32 v5, v5, s73, v184
	v_mov_b32_e32 v22, v143
	v_cvt_pk_fp8_f32 v22, v26, v27
	v_pk_add_f32 v[14:15], v[14:15], 1.0 op_sel_hi:[1,0]
	v_cvt_pk_fp8_f32 v22, v28, v29 op_sel:[0,0,1]
	ds_write_b64 v122, v[22:23]
	s_nop 0
	v_pk_mul_f32 v[2:3], v[2:3], v[6:7]
	v_med3_f32 v6, v8, s70, v167
	v_med3_f32 v7, v9, s70, v167
	v_exp_f32_e64 v8, -v4
	v_exp_f32_e64 v9, -v5
	s_nop 0
	v_pk_add_f32 v[8:9], v[8:9], 1.0 op_sel_hi:[1,0]
	s_nop 0
	v_pk_mul_f32 v[180:181], v[14:15], v[8:9]
	v_rcp_f32_e32 v180, v180
	v_rcp_f32_e32 v181, v181
	s_nop 0
	v_pk_mul_f32 v[182:183], v[180:181], v[8:9]
	v_pk_mul_f32 v[8:9], v[180:181], v[14:15]
	v_pk_mul_f32 v[2:3], v[2:3], v[182:183]
	s_nop 0
	v_pk_mul_f32 v[4:5], v[4:5], v[8:9]
	s_nop 0
	v_pk_mul_f32 v[4:5], v[4:5], v[6:7]
	v_mov_b32_e32 v6, v143
	v_mov_b32_e32 v7, v143
	v_cvt_pk_fp8_f32 v6, v10, v11
	v_cvt_pk_fp8_f32 v7, v2, v3
	v_cvt_pk_fp8_f32 v6, v12, v13 op_sel:[0,0,1]
	v_cvt_pk_fp8_f32 v7, v4, v5 op_sel:[0,0,1]
	ds_write_b64 v122, v[6:7] offset:768
	v_add_u32_e32 v6, 0xa0, v106
	ds_read_b128 v[2:5], v108
	v_ashrrev_i32_e32 v7, 31, v6
	v_lshl_add_u32 v6, v6, 10, v142
	s_add_u32 s86, s16, s8
	s_addc_u32 s87, s17, s9
	s_mov_b64 s[8:9], -1
	s_waitcnt lgkmcnt(0)
	global_store_dwordx4 v6, v[2:5], s[86:87]
	s_cbranch_vccnz .LBB0_1537
	s_lshl_b64 s[6:7], s[74:75], 12
	s_add_u32 s9, s33, s6
	s_addc_u32 s69, s54, s7
	s_lshl_b32 s6, s68, 7
	s_ashr_i32 s7, s6, 31
	v_mov_b32_e32 v2, v0
	s_lshl_b64 s[6:7], s[6:7], 1
	s_add_u32 s6, s9, s6
	v_readfirstlane_b32 s8, v2
	s_addc_u32 s7, s69, s7
	s_and_b32 s9, s8, 0xc0
	s_add_u32 s6, s6, s9
	s_addc_u32 s7, s7, 0
	v_and_b32_e32 v3, 48, v2
	global_load_dwordx4 v[86:89], v3, s[6:7]
	global_load_dwordx4 v[82:85], v3, s[6:7] offset:2048
	s_ashr_i32 s7, s8, 2
	s_lshl_b32 s6, s72, 8
	s_andn2_b32 s7, s7, 63
	s_add_i32 s7, s7, s6
	v_and_or_b32 v2, v2, 15, s7
	v_lshlrev_b32_e32 v4, 2, v2
	global_load_dword v177, v4, s[12:13] offset:0
	global_load_dword v176, v4, s[12:13] offset:64
	global_load_dword v175, v4, s[12:13] offset:128
	global_load_dword v174, v4, s[12:13] offset:192
	global_load_dword v173, v4, s[12:13] offset:512
	global_load_dword v172, v4, s[12:13] offset:576
	global_load_dword v171, v4, s[12:13] offset:640
	global_load_dword v168, v4, s[12:13] offset:704
	s_andn2_b64 vcc, exec, s[14:15]
	s_cbranch_vccnz .LBB0_1536
	s_barrier
	s_branch .LBB0_1536

.LBB0_3348:
	s_mov_b32 s82, 0xc2700000
	v_mov_b32_e32 v190, 0x41898193
	v_lshlrev_b32_e32 v160, 16, v46
	v_and_b32_e32 v161, 0xffff0000, v46
	v_lshlrev_b32_e32 v156, 16, v42
	v_and_b32_e32 v157, 0xffff0000, v42
	v_mul_f32_e32 v42, 0x3d800000, v179
	v_lshlrev_b32_e32 v154, 16, v47
	v_and_b32_e32 v155, 0xffff0000, v47
	v_lshlrev_b32_e32 v46, 16, v44
	v_and_b32_e32 v47, 0xffff0000, v44
	v_lshlrev_b32_e32 v150, 16, v45
	v_and_b32_e32 v151, 0xffff0000, v45
	v_pk_fma_f32 v[44:45], v[42:43], v[130:131], v[160:161] op_sel_hi:[0,1,1]
	v_med3_f32 v44, v44, s82, v190
	v_med3_f32 v45, v45, s82, v190
	v_exp_f32_e64 v130, -v44
	v_exp_f32_e64 v131, -v45
	v_pk_fma_f32 v[132:133], v[42:43], v[132:133], v[154:155] op_sel_hi:[0,1,1]
	v_med3_f32 v132, v132, s82, v190
	v_med3_f32 v133, v133, s82, v190
	v_pk_add_f32 v[130:131], v[130:131], 1.0 op_sel_hi:[1,0]
	v_exp_f32_e64 v188, -v132
	v_exp_f32_e64 v189, -v133
	v_lshlrev_b32_e32 v152, 16, v48
	v_and_b32_e32 v153, 0xffff0000, v48
	v_pk_add_f32 v[188:189], v[188:189], 1.0 op_sel_hi:[1,0]
	v_pk_fma_f32 v[122:123], v[42:43], v[122:123], v[152:153] op_sel_hi:[0,1,1]
	v_pk_mul_f32 v[184:185], v[130:131], v[188:189]
	v_rcp_f32_e32 v184, v184
	v_rcp_f32_e32 v185, v185
	s_nop 0
	v_pk_mul_f32 v[186:187], v[184:185], v[188:189]
	v_pk_mul_f32 v[188:189], v[184:185], v[130:131]
	v_pk_mul_f32 v[44:45], v[44:45], v[186:187]
	v_med3_f32 v122, v122, s82, v190
	v_med3_f32 v123, v123, s82, v190
	v_lshlrev_b32_e32 v48, 16, v49
	v_pk_mul_f32 v[130:131], v[132:133], v[188:189]
	v_exp_f32_e64 v132, -v122
	v_exp_f32_e64 v133, -v123
	v_and_b32_e32 v49, 0xffff0000, v49
	v_pk_fma_f32 v[124:125], v[42:43], v[124:125], v[48:49] op_sel_hi:[0,1,1]
	v_lshlrev_b32_e32 v158, 16, v43
	v_and_b32_e32 v159, 0xffff0000, v43
	v_med3_f32 v124, v124, s82, v190
	v_med3_f32 v125, v125, s82, v190
	v_pk_fma_f32 v[136:137], v[42:43], v[136:137], v[158:159] op_sel_hi:[0,1,1]
	v_pk_fma_f32 v[134:135], v[42:43], v[134:135], v[156:157] op_sel_hi:[0,1,1]
	v_pk_fma_f32 v[128:129], v[42:43], v[128:129], v[150:151] op_sel_hi:[0,1,1]
	v_pk_add_f32 v[132:133], v[132:133], 1.0 op_sel_hi:[1,0]
	v_pk_fma_f32 v[42:43], v[42:43], v[126:127], v[46:47] op_sel_hi:[0,1,1]
	v_exp_f32_e64 v188, -v124
	v_exp_f32_e64 v189, -v125
	v_med3_f32 v42, v42, s81, v170
	v_pk_add_f32 v[188:189], v[188:189], 1.0 op_sel_hi:[1,0]
	v_med3_f32 v43, v43, s81, v170
	v_pk_mul_f32 v[184:185], v[132:133], v[188:189]
	v_rcp_f32_e32 v184, v184
	v_rcp_f32_e32 v185, v185
	s_nop 0
	v_pk_mul_f32 v[186:187], v[184:185], v[188:189]
	v_pk_mul_f32 v[188:189], v[184:185], v[132:133]
	v_pk_mul_f32 v[122:123], v[122:123], v[186:187]
	v_pk_mul_f32 v[42:43], v[122:123], v[42:43]
	v_med3_f32 v123, v129, s81, v170
	v_mov_b32_e32 v129, 0
	v_cvt_pk_fp8_f32 v129, v42, v43
	v_med3_f32 v122, v128, s81, v170
	v_pk_mul_f32 v[42:43], v[124:125], v[188:189]
	v_med3_f32 v134, v134, s81, v170
	v_med3_f32 v135, v135, s81, v170
	v_pk_mul_f32 v[42:43], v[42:43], v[122:123]
	v_pk_mul_f32 v[44:45], v[44:45], v[134:135]
	v_mov_b32_e32 v128, 0
	v_cvt_pk_fp8_f32 v129, v42, v43 op_sel:[0,0,1]
	v_mul_f32_e32 v42, 0x3d800000, v178
	v_cvt_pk_fp8_f32 v128, v44, v45
	v_pk_fma_f32 v[44:45], v[42:43], v[114:115], v[160:161] op_sel_hi:[0,1,1]
	v_med3_f32 v44, v44, s82, v190
	v_med3_f32 v45, v45, s82, v190
	v_exp_f32_e64 v114, -v44
	v_exp_f32_e64 v115, -v45
	v_pk_fma_f32 v[116:117], v[42:43], v[116:117], v[154:155] op_sel_hi:[0,1,1]
	v_med3_f32 v116, v116, s82, v190
	v_med3_f32 v117, v117, s82, v190
	v_pk_add_f32 v[114:115], v[114:115], 1.0 op_sel_hi:[1,0]
	v_exp_f32_e64 v188, -v116
	v_exp_f32_e64 v189, -v117
	v_pk_fma_f32 v[106:107], v[42:43], v[106:107], v[152:153] op_sel_hi:[0,1,1]
	v_med3_f32 v106, v106, s82, v190
	v_pk_add_f32 v[188:189], v[188:189], 1.0 op_sel_hi:[1,0]
	v_med3_f32 v107, v107, s82, v190
	v_pk_mul_f32 v[184:185], v[114:115], v[188:189]
	v_rcp_f32_e32 v184, v184
	v_rcp_f32_e32 v185, v185
	s_nop 0
	v_pk_mul_f32 v[186:187], v[184:185], v[188:189]
	v_pk_mul_f32 v[188:189], v[184:185], v[114:115]
	v_pk_mul_f32 v[44:45], v[44:45], v[186:187]
	v_pk_fma_f32 v[108:109], v[42:43], v[108:109], v[48:49] op_sel_hi:[0,1,1]
	v_med3_f32 v108, v108, s82, v190
	v_med3_f32 v109, v109, s82, v190
	v_pk_mul_f32 v[114:115], v[116:117], v[188:189]
	v_exp_f32_e64 v116, -v106
	v_exp_f32_e64 v117, -v107
	v_pk_fma_f32 v[120:121], v[42:43], v[120:121], v[158:159] op_sel_hi:[0,1,1]
	v_pk_fma_f32 v[118:119], v[42:43], v[118:119], v[156:157] op_sel_hi:[0,1,1]
	v_pk_fma_f32 v[112:113], v[42:43], v[112:113], v[150:151] op_sel_hi:[0,1,1]
	v_pk_add_f32 v[116:117], v[116:117], 1.0 op_sel_hi:[1,0]
	v_pk_fma_f32 v[42:43], v[42:43], v[110:111], v[46:47] op_sel_hi:[0,1,1]
	v_exp_f32_e64 v188, -v108
	v_exp_f32_e64 v189, -v109
	v_med3_f32 v118, v118, s81, v170
	v_pk_add_f32 v[188:189], v[188:189], 1.0 op_sel_hi:[1,0]
	v_med3_f32 v119, v119, s81, v170
	v_med3_f32 v42, v42, s81, v170
	v_med3_f32 v43, v43, s81, v170
	v_pk_mul_f32 v[184:185], v[116:117], v[188:189]
	v_rcp_f32_e32 v184, v184
	v_rcp_f32_e32 v185, v185
	s_nop 0
	v_pk_mul_f32 v[186:187], v[184:185], v[188:189]
	v_pk_mul_f32 v[188:189], v[184:185], v[116:117]
	v_pk_mul_f32 v[106:107], v[106:107], v[186:187]
	v_pk_mul_f32 v[44:45], v[44:45], v[118:119]
	v_pk_mul_f32 v[42:43], v[106:107], v[42:43]
	v_med3_f32 v106, v112, s81, v170
	v_med3_f32 v107, v113, s81, v170
	v_mov_b32_e32 v112, 0
	v_mov_b32_e32 v113, 0
	v_mov_b32_e32 v142, v0
	v_cvt_pk_fp8_f32 v112, v44, v45
	v_cvt_pk_fp8_f32 v113, v42, v43
	v_med3_f32 v134, v136, s81, v170
	v_readfirstlane_b32 s65, v142
	v_med3_f32 v135, v137, s81, v170
	s_ashr_i32 s10, s65, 6
	v_pk_mul_f32 v[130:131], v[130:131], v[134:135]
	v_med3_f32 v118, v120, s81, v170
	v_med3_f32 v119, v121, s81, v170
	v_pk_mul_f32 v[42:43], v[108:109], v[188:189]
	s_mul_i32 s11, s10, 0xb00
	v_cvt_pk_fp8_f32 v128, v130, v131 op_sel:[0,0,1]
	v_pk_mul_f32 v[114:115], v[114:115], v[118:119]
	v_pk_mul_f32 v[42:43], v[42:43], v[106:107]
	s_add_i32 s67, s11, 0
	v_and_b32_e32 v147, 15, v142
	v_lshrrev_b32_e32 v125, 1, v142
	v_cvt_pk_fp8_f32 v112, v114, v115 op_sel:[0,0,1]
	v_cvt_pk_fp8_f32 v113, v42, v43 op_sel:[0,0,1]
	s_add_i32 s67, s67, 0x20000
	v_mul_u32_u24_e32 v124, 48, v147
	v_and_b32_e32 v42, 24, v125
	v_add3_u32 v108, s67, v124, v42
	ds_write_b64 v108, v[128:129]
	ds_write_b64 v108, v[112:113] offset:768
	v_mul_f32_e32 v112, 0x3d800000, v177
	v_pk_fma_f32 v[98:99], v[112:113], v[98:99], v[160:161] op_sel_hi:[0,1,1]
	v_med3_f32 v98, v98, s82, v190
	v_med3_f32 v99, v99, s82, v190
	v_exp_f32_e64 v114, -v98
	v_exp_f32_e64 v115, -v99
	v_pk_fma_f32 v[100:101], v[112:113], v[100:101], v[154:155] op_sel_hi:[0,1,1]
	v_med3_f32 v100, v100, s82, v190
	v_med3_f32 v101, v101, s82, v190
	v_pk_add_f32 v[114:115], v[114:115], 1.0 op_sel_hi:[1,0]
	v_exp_f32_e64 v188, -v100
	v_exp_f32_e64 v189, -v101
	v_pk_fma_f32 v[102:103], v[112:113], v[102:103], v[156:157] op_sel_hi:[0,1,1]
	v_pk_fma_f32 v[90:91], v[112:113], v[90:91], v[152:153] op_sel_hi:[0,1,1]
	v_pk_add_f32 v[188:189], v[188:189], 1.0 op_sel_hi:[1,0]
	v_pk_fma_f32 v[104:105], v[112:113], v[104:105], v[158:159] op_sel_hi:[0,1,1]
	v_med3_f32 v102, v102, s81, v170
	v_med3_f32 v103, v103, s81, v170
	v_pk_mul_f32 v[184:185], v[114:115], v[188:189]
	v_rcp_f32_e32 v184, v184
	v_rcp_f32_e32 v185, v185
	s_nop 0
	v_pk_mul_f32 v[186:187], v[184:185], v[188:189]
	v_pk_mul_f32 v[188:189], v[184:185], v[114:115]
	v_pk_mul_f32 v[98:99], v[98:99], v[186:187]
	v_med3_f32 v90, v90, s82, v190
	v_med3_f32 v91, v91, s82, v190
	v_pk_mul_f32 v[98:99], v[98:99], v[102:103]
	v_med3_f32 v102, v104, s81, v170
	v_med3_f32 v103, v105, s81, v170
	v_exp_f32_e64 v104, -v90
	v_exp_f32_e64 v105, -v91
	v_pk_mul_f32 v[100:101], v[100:101], v[188:189]
	v_pk_fma_f32 v[92:93], v[112:113], v[92:93], v[48:49] op_sel_hi:[0,1,1]
	v_pk_mul_f32 v[100:101], v[100:101], v[102:103]
	v_pk_add_f32 v[102:103], v[104:105], 1.0 op_sel_hi:[1,0]
	v_med3_f32 v92, v92, s82, v190
	v_rcp_f32_e32 v102, v102
	v_rcp_f32_e32 v103, v103
	v_med3_f32 v93, v93, s82, v190
	v_pk_fma_f32 v[94:95], v[112:113], v[94:95], v[46:47] op_sel_hi:[0,1,1]
	v_pk_fma_f32 v[96:97], v[112:113], v[96:97], v[150:151] op_sel_hi:[0,1,1]
	v_pk_mul_f32 v[90:91], v[90:91], v[102:103]
	v_exp_f32_e64 v102, -v92
	v_exp_f32_e64 v103, -v93
	v_med3_f32 v94, v94, s81, v170
	v_med3_f32 v95, v95, s81, v170
	v_pk_mul_f32 v[90:91], v[90:91], v[94:95]
	v_med3_f32 v94, v96, s81, v170
	v_med3_f32 v95, v97, s81, v170
	v_pk_add_f32 v[96:97], v[102:103], 1.0 op_sel_hi:[1,0]
	v_mov_b32_e32 v103, v143
	v_rcp_f32_e32 v96, v96
	v_rcp_f32_e32 v97, v97
	v_cvt_pk_fp8_f32 v103, v90, v91
	v_mov_b32_e32 v102, v143
	v_bfe_u32 v106, v142, 1, 5
	v_pk_mul_f32 v[90:91], v[92:93], v[96:97]
	v_lshlrev_b32_e32 v43, 4, v142
	v_pk_mul_f32 v[90:91], v[90:91], v[94:95]
	s_ashr_i32 s65, s65, 2
	v_cvt_pk_fp8_f32 v103, v90, v91 op_sel:[0,0,1]
	v_mul_f32_e32 v90, 0x3d800000, v176
	v_pk_fma_f32 v[82:83], v[90:91], v[82:83], v[160:161] op_sel_hi:[0,1,1]
	v_med3_f32 v82, v82, s82, v190
	v_med3_f32 v83, v83, s82, v190
	v_exp_f32_e64 v92, -v82
	v_exp_f32_e64 v93, -v83
	v_pk_fma_f32 v[84:85], v[90:91], v[84:85], v[154:155] op_sel_hi:[0,1,1]
	v_med3_f32 v84, v84, s82, v190
	v_med3_f32 v85, v85, s82, v190
	v_pk_add_f32 v[92:93], v[92:93], 1.0 op_sel_hi:[1,0]
	v_exp_f32_e64 v188, -v84
	v_exp_f32_e64 v189, -v85
	v_pk_fma_f32 v[86:87], v[90:91], v[86:87], v[156:157] op_sel_hi:[0,1,1]
	v_pk_fma_f32 v[66:67], v[90:91], v[66:67], v[152:153] op_sel_hi:[0,1,1]
	v_pk_add_f32 v[188:189], v[188:189], 1.0 op_sel_hi:[1,0]
	v_pk_fma_f32 v[88:89], v[90:91], v[88:89], v[158:159] op_sel_hi:[0,1,1]
	v_med3_f32 v86, v86, s81, v170
	v_med3_f32 v87, v87, s81, v170
	v_pk_mul_f32 v[184:185], v[92:93], v[188:189]
	v_rcp_f32_e32 v184, v184
	v_rcp_f32_e32 v185, v185
	s_nop 0
	v_pk_mul_f32 v[186:187], v[184:185], v[188:189]
	v_pk_mul_f32 v[188:189], v[184:185], v[92:93]
	v_pk_mul_f32 v[82:83], v[82:83], v[186:187]
	v_med3_f32 v66, v66, s82, v190
	v_med3_f32 v67, v67, s82, v190
	v_pk_mul_f32 v[82:83], v[82:83], v[86:87]
	v_med3_f32 v86, v88, s81, v170
	v_med3_f32 v87, v89, s81, v170
	v_exp_f32_e64 v88, -v66
	v_exp_f32_e64 v89, -v67
	v_pk_mul_f32 v[84:85], v[84:85], v[188:189]
	v_pk_fma_f32 v[68:69], v[90:91], v[68:69], v[48:49] op_sel_hi:[0,1,1]
	v_pk_mul_f32 v[84:85], v[84:85], v[86:87]
	v_pk_add_f32 v[86:87], v[88:89], 1.0 op_sel_hi:[1,0]
	v_med3_f32 v68, v68, s82, v190
	v_rcp_f32_e32 v86, v86
	v_rcp_f32_e32 v87, v87
	v_med3_f32 v69, v69, s82, v190
	v_pk_fma_f32 v[74:75], v[90:91], v[74:75], v[46:47] op_sel_hi:[0,1,1]
	v_pk_fma_f32 v[76:77], v[90:91], v[76:77], v[150:151] op_sel_hi:[0,1,1]
	v_pk_mul_f32 v[66:67], v[66:67], v[86:87]
	v_exp_f32_e64 v86, -v68
	v_exp_f32_e64 v87, -v69
	v_med3_f32 v74, v74, s81, v170
	v_med3_f32 v75, v75, s81, v170
	v_pk_mul_f32 v[66:67], v[66:67], v[74:75]
	v_med3_f32 v74, v76, s81, v170
	v_med3_f32 v75, v77, s81, v170
	v_pk_add_f32 v[76:77], v[86:87], 1.0 op_sel_hi:[1,0]
	v_mov_b32_e32 v87, v143
	v_rcp_f32_e32 v76, v76
	v_rcp_f32_e32 v77, v77
	v_cvt_pk_fp8_f32 v87, v66, v67
	v_cvt_pk_fp8_f32 v102, v98, v99
	v_mov_b32_e32 v86, v143
	v_pk_mul_f32 v[66:67], v[68:69], v[76:77]
	v_mul_f32_e32 v68, 0x3d800000, v175
	v_pk_fma_f32 v[70:71], v[68:69], v[70:71], v[160:161] op_sel_hi:[0,1,1]
	v_med3_f32 v70, v70, s82, v190
	v_med3_f32 v71, v71, s82, v190
	v_pk_mul_f32 v[66:67], v[66:67], v[74:75]
	v_exp_f32_e64 v74, -v70
	v_exp_f32_e64 v75, -v71
	v_pk_fma_f32 v[72:73], v[68:69], v[72:73], v[154:155] op_sel_hi:[0,1,1]
	v_med3_f32 v72, v72, s82, v190
	v_med3_f32 v73, v73, s82, v190
	v_pk_add_f32 v[74:75], v[74:75], 1.0 op_sel_hi:[1,0]
	v_pk_fma_f32 v[76:77], v[68:69], v[80:81], v[158:159] op_sel_hi:[0,1,1]
	v_exp_f32_e64 v188, -v72
	v_exp_f32_e64 v189, -v73
	v_pk_fma_f32 v[58:59], v[68:69], v[58:59], v[152:153] op_sel_hi:[0,1,1]
	v_med3_f32 v58, v58, s82, v190
	v_pk_add_f32 v[188:189], v[188:189], 1.0 op_sel_hi:[1,0]
	v_med3_f32 v59, v59, s82, v190
	v_pk_mul_f32 v[184:185], v[74:75], v[188:189]
	v_rcp_f32_e32 v184, v184
	v_rcp_f32_e32 v185, v185
	s_nop 0
	v_pk_mul_f32 v[186:187], v[184:185], v[188:189]
	v_pk_mul_f32 v[188:189], v[184:185], v[74:75]
	v_pk_mul_f32 v[70:71], v[70:71], v[186:187]
	v_pk_fma_f32 v[60:61], v[68:69], v[60:61], v[48:49] op_sel_hi:[0,1,1]
	v_med3_f32 v60, v60, s82, v190
	v_med3_f32 v61, v61, s82, v190
	v_pk_mul_f32 v[72:73], v[72:73], v[188:189]
	v_exp_f32_e64 v74, -v58
	v_exp_f32_e64 v75, -v59
	v_pk_fma_f32 v[78:79], v[68:69], v[78:79], v[156:157] op_sel_hi:[0,1,1]
	v_pk_fma_f32 v[64:65], v[68:69], v[64:65], v[150:151] op_sel_hi:[0,1,1]
	v_pk_fma_f32 v[62:63], v[68:69], v[62:63], v[46:47] op_sel_hi:[0,1,1]
	v_pk_add_f32 v[74:75], v[74:75], 1.0 op_sel_hi:[1,0]
	v_exp_f32_e64 v188, -v60
	v_exp_f32_e64 v189, -v61
	v_med3_f32 v62, v62, s81, v170
	v_med3_f32 v63, v63, s81, v170
	v_mul_u32_u24_e32 v42, 48, v106
	v_pk_mul_f32 v[58:59], v[58:59], v[62:63]
	v_med3_f32 v62, v64, s81, v170
	v_med3_f32 v63, v65, s81, v170
	v_pk_add_f32 v[188:189], v[188:189], 1.0 op_sel_hi:[1,0]
	v_mov_b32_e32 v69, v143
	v_pk_mul_f32 v[184:185], v[74:75], v[188:189]
	v_rcp_f32_e32 v184, v184
	v_rcp_f32_e32 v185, v185
	s_nop 0
	v_pk_mul_f32 v[186:187], v[184:185], v[188:189]
	v_pk_mul_f32 v[188:189], v[184:185], v[74:75]
	v_pk_mul_f32 v[58:59], v[58:59], v[186:187]
	v_cvt_pk_fp8_f32 v69, v58, v59
	v_and_b32_e32 v142, 16, v43
	s_andn2_b32 s65, s65, 63
	v_pk_mul_f32 v[58:59], v[60:61], v[188:189]
	v_lshl_or_b32 v106, s74, 8, v106
	v_pk_mul_f32 v[58:59], v[58:59], v[62:63]
	v_cvt_pk_fp8_f32 v86, v82, v83
	v_cvt_pk_fp8_f32 v69, v58, v59 op_sel:[0,0,1]
	v_mul_f32_e32 v58, 0x3d800000, v174
	v_pk_fma_f32 v[50:51], v[58:59], v[50:51], v[160:161] op_sel_hi:[0,1,1]
	v_med3_f32 v50, v50, s82, v190
	v_med3_f32 v51, v51, s82, v190
	v_exp_f32_e64 v60, -v50
	v_exp_f32_e64 v61, -v51
	v_pk_fma_f32 v[52:53], v[58:59], v[52:53], v[154:155] op_sel_hi:[0,1,1]
	v_med3_f32 v52, v52, s82, v190
	v_med3_f32 v53, v53, s82, v190
	v_pk_add_f32 v[60:61], v[60:61], 1.0 op_sel_hi:[1,0]
	v_exp_f32_e64 v188, -v52
	v_exp_f32_e64 v189, -v53
	v_pk_fma_f32 v[54:55], v[58:59], v[54:55], v[156:157] op_sel_hi:[0,1,1]
	v_pk_fma_f32 v[34:35], v[58:59], v[34:35], v[152:153] op_sel_hi:[0,1,1]
	v_pk_add_f32 v[188:189], v[188:189], 1.0 op_sel_hi:[1,0]
	v_pk_fma_f32 v[56:57], v[58:59], v[56:57], v[158:159] op_sel_hi:[0,1,1]
	v_med3_f32 v54, v54, s81, v170
	v_med3_f32 v55, v55, s81, v170
	v_pk_mul_f32 v[184:185], v[60:61], v[188:189]
	v_rcp_f32_e32 v184, v184
	v_rcp_f32_e32 v185, v185
	s_nop 0
	v_pk_mul_f32 v[186:187], v[184:185], v[188:189]
	v_pk_mul_f32 v[188:189], v[184:185], v[60:61]
	v_pk_mul_f32 v[50:51], v[50:51], v[186:187]
	v_med3_f32 v34, v34, s82, v190
	v_med3_f32 v35, v35, s82, v190
	v_pk_mul_f32 v[50:51], v[50:51], v[54:55]
	v_med3_f32 v54, v56, s81, v170
	v_med3_f32 v55, v57, s81, v170
	v_exp_f32_e64 v56, -v34
	v_exp_f32_e64 v57, -v35
	v_pk_mul_f32 v[52:53], v[52:53], v[188:189]
	v_pk_fma_f32 v[36:37], v[58:59], v[36:37], v[48:49] op_sel_hi:[0,1,1]
	v_pk_mul_f32 v[52:53], v[52:53], v[54:55]
	v_pk_add_f32 v[54:55], v[56:57], 1.0 op_sel_hi:[1,0]
	v_med3_f32 v36, v36, s82, v190
	v_med3_f32 v37, v37, s82, v190
	s_lshl_b32 s10, s10, 5
	v_add3_u32 v109, s67, v42, v142
	v_add_u32_e32 v106, s65, v106
	v_exp_f32_e64 v188, -v36
	v_exp_f32_e64 v189, -v37
	s_lshl_b32 s11, s76, 7
	s_and_b32 s10, s10, 0x60
	ds_read_b128 v[42:45], v109
	v_ashrrev_i32_e32 v107, 31, v106
	s_or_b32 s10, s10, s11
	v_lshl_add_u32 v110, v106, 10, v142
	v_cvt_pk_fp8_f32 v102, v100, v101 op_sel:[0,0,1]
	v_pk_fma_f32 v[38:39], v[58:59], v[38:39], v[46:47] op_sel_hi:[0,1,1]
	s_ashr_i32 s11, s10, 31
	v_cvt_pk_fp8_f32 v86, v84, v85 op_sel:[0,0,1]
	v_cvt_pk_fp8_f32 v87, v66, v67 op_sel:[0,0,1]
	v_pk_fma_f32 v[40:41], v[58:59], v[40:41], v[150:151] op_sel_hi:[0,1,1]
	v_med3_f32 v38, v38, s81, v170
	v_med3_f32 v39, v39, s81, v170
	s_add_u32 s86, s18, s10
	s_addc_u32 s87, s19, s11
	v_pk_mul_f32 v[34:35], v[34:35], v[38:39]
	v_med3_f32 v38, v40, s81, v170
	v_med3_f32 v39, v41, s81, v170
	v_pk_add_f32 v[188:189], v[188:189], 1.0 op_sel_hi:[1,0]
	v_mov_b32_e32 v66, v110
	v_pk_mul_f32 v[184:185], v[54:55], v[188:189]
	v_rcp_f32_e32 v184, v184
	v_rcp_f32_e32 v185, v185
	s_nop 0
	v_pk_mul_f32 v[186:187], v[184:185], v[188:189]
	v_pk_mul_f32 v[188:189], v[184:185], v[54:55]
	v_pk_mul_f32 v[34:35], v[34:35], v[186:187]
	s_waitcnt lgkmcnt(0)
	global_store_dwordx4 v66, v[42:45], s[86:87]
	ds_write_b64 v108, v[102:103]
	ds_write_b64 v108, v[86:87] offset:768
	v_or_b32_e32 v66, 32, v106
	v_mov_b32_e32 v55, v143
	ds_read_b128 v[42:45], v109
	v_ashrrev_i32_e32 v67, 31, v66
	v_cvt_pk_fp8_f32 v55, v34, v35
	v_lshl_add_u32 v66, v66, 10, v142
	v_pk_mul_f32 v[34:35], v[36:37], v[188:189]
	v_mul_f32_e32 v40, 0x3d800000, v171
	s_add_u32 s86, s18, s10
	s_addc_u32 s87, s19, s11
	v_pk_mul_f32 v[34:35], v[34:35], v[38:39]
	v_pk_fma_f32 v[26:27], v[40:41], v[26:27], v[160:161] op_sel_hi:[0,1,1]
	v_cvt_pk_fp8_f32 v55, v34, v35 op_sel:[0,0,1]
	v_mov_b32_e32 v34, v66
	v_med3_f32 v26, v26, s82, v190
	v_med3_f32 v27, v27, s82, v190
	s_waitcnt lgkmcnt(0)
	global_store_dwordx4 v34, v[42:45], s[86:87]
	v_pk_fma_f32 v[28:29], v[40:41], v[28:29], v[154:155] op_sel_hi:[0,1,1]
	v_med3_f32 v28, v28, s82, v190
	v_exp_f32_e64 v42, -v26
	v_exp_f32_e64 v43, -v27
	v_med3_f32 v29, v29, s82, v190
	v_exp_f32_e64 v188, -v28
	v_exp_f32_e64 v189, -v29
	v_pk_add_f32 v[42:43], v[42:43], 1.0 op_sel_hi:[1,0]
	v_pk_fma_f32 v[30:31], v[40:41], v[30:31], v[156:157] op_sel_hi:[0,1,1]
	v_pk_fma_f32 v[18:19], v[40:41], v[18:19], v[152:153] op_sel_hi:[0,1,1]
	v_pk_fma_f32 v[32:33], v[40:41], v[32:33], v[158:159] op_sel_hi:[0,1,1]
	v_med3_f32 v30, v30, s81, v170
	v_pk_add_f32 v[188:189], v[188:189], 1.0 op_sel_hi:[1,0]
	v_med3_f32 v31, v31, s81, v170
	v_pk_mul_f32 v[184:185], v[42:43], v[188:189]
	v_rcp_f32_e32 v184, v184
	v_rcp_f32_e32 v185, v185
	s_nop 0
	v_pk_mul_f32 v[186:187], v[184:185], v[188:189]
	v_pk_mul_f32 v[188:189], v[184:185], v[42:43]
	v_pk_mul_f32 v[26:27], v[26:27], v[186:187]
	v_med3_f32 v18, v18, s82, v190
	v_med3_f32 v19, v19, s82, v190
	v_pk_mul_f32 v[26:27], v[26:27], v[30:31]
	v_med3_f32 v30, v32, s81, v170
	v_med3_f32 v31, v33, s81, v170
	v_exp_f32_e64 v32, -v18
	v_exp_f32_e64 v33, -v19
	v_pk_mul_f32 v[28:29], v[28:29], v[188:189]
	v_pk_fma_f32 v[20:21], v[40:41], v[20:21], v[48:49] op_sel_hi:[0,1,1]
	v_pk_mul_f32 v[28:29], v[28:29], v[30:31]
	v_pk_add_f32 v[30:31], v[32:33], 1.0 op_sel_hi:[1,0]
	v_med3_f32 v20, v20, s82, v190
	v_rcp_f32_e32 v30, v30
	v_rcp_f32_e32 v31, v31
	v_med3_f32 v21, v21, s82, v190
	v_pk_fma_f32 v[22:23], v[40:41], v[22:23], v[46:47] op_sel_hi:[0,1,1]
	v_pk_fma_f32 v[24:25], v[40:41], v[24:25], v[150:151] op_sel_hi:[0,1,1]
	v_pk_mul_f32 v[18:19], v[18:19], v[30:31]
	v_exp_f32_e64 v30, -v20
	v_exp_f32_e64 v31, -v21
	v_med3_f32 v22, v22, s81, v170
	v_med3_f32 v23, v23, s81, v170
	v_pk_mul_f32 v[18:19], v[18:19], v[22:23]
	v_med3_f32 v22, v24, s81, v170
	v_med3_f32 v23, v25, s81, v170
	v_pk_add_f32 v[24:25], v[30:31], 1.0 op_sel_hi:[1,0]
	v_mov_b32_e32 v31, v143
	v_rcp_f32_e32 v24, v24
	v_rcp_f32_e32 v25, v25
	v_cvt_pk_fp8_f32 v31, v18, v19
	v_med3_f32 v78, v78, s81, v170
	v_med3_f32 v79, v79, s81, v170
	v_pk_mul_f32 v[18:19], v[20:21], v[24:25]
	v_pk_mul_f32 v[70:71], v[70:71], v[78:79]
	v_pk_mul_f32 v[18:19], v[18:19], v[22:23]
	v_mov_b32_e32 v68, v143
	v_cvt_pk_fp8_f32 v31, v18, v19 op_sel:[0,0,1]
	v_mul_f32_e32 v18, 0x3d800000, v169
	v_pk_fma_f32 v[10:11], v[18:19], v[10:11], v[160:161] op_sel_hi:[0,1,1]
	v_med3_f32 v10, v10, s82, v190
	v_med3_f32 v11, v11, s82, v190
	v_exp_f32_e64 v20, -v10
	v_exp_f32_e64 v21, -v11
	v_pk_fma_f32 v[12:13], v[18:19], v[12:13], v[154:155] op_sel_hi:[0,1,1]
	v_med3_f32 v12, v12, s82, v190
	v_med3_f32 v13, v13, s82, v190
	v_pk_add_f32 v[20:21], v[20:21], 1.0 op_sel_hi:[1,0]
	v_exp_f32_e64 v188, -v12
	v_exp_f32_e64 v189, -v13
	v_pk_fma_f32 v[14:15], v[18:19], v[14:15], v[156:157] op_sel_hi:[0,1,1]
	v_pk_fma_f32 v[2:3], v[18:19], v[2:3], v[152:153] op_sel_hi:[0,1,1]
	v_pk_add_f32 v[188:189], v[188:189], 1.0 op_sel_hi:[1,0]
	v_pk_fma_f32 v[16:17], v[18:19], v[16:17], v[158:159] op_sel_hi:[0,1,1]
	v_med3_f32 v14, v14, s81, v170
	v_med3_f32 v15, v15, s81, v170
	v_pk_mul_f32 v[184:185], v[20:21], v[188:189]
	v_rcp_f32_e32 v184, v184
	v_rcp_f32_e32 v185, v185
	s_nop 0
	v_pk_mul_f32 v[186:187], v[184:185], v[188:189]
	v_pk_mul_f32 v[188:189], v[184:185], v[20:21]
	v_pk_mul_f32 v[10:11], v[10:11], v[186:187]
	v_med3_f32 v2, v2, s82, v190
	v_med3_f32 v3, v3, s82, v190
	v_pk_mul_f32 v[10:11], v[10:11], v[14:15]
	v_med3_f32 v14, v16, s81, v170
	v_med3_f32 v15, v17, s81, v170
	v_exp_f32_e64 v16, -v2
	v_exp_f32_e64 v17, -v3
	v_pk_mul_f32 v[12:13], v[12:13], v[188:189]
	v_pk_fma_f32 v[4:5], v[18:19], v[4:5], v[48:49] op_sel_hi:[0,1,1]
	v_pk_mul_f32 v[12:13], v[12:13], v[14:15]
	v_pk_add_f32 v[14:15], v[16:17], 1.0 op_sel_hi:[1,0]
	v_med3_f32 v4, v4, s82, v190
	v_med3_f32 v5, v5, s82, v190
	v_cvt_pk_fp8_f32 v68, v70, v71
	v_mov_b32_e32 v54, v143
	v_exp_f32_e64 v188, -v4
	v_exp_f32_e64 v189, -v5
	v_cvt_pk_fp8_f32 v54, v50, v51
	v_med3_f32 v76, v76, s81, v170
	v_med3_f32 v77, v77, s81, v170
	v_pk_fma_f32 v[6:7], v[18:19], v[6:7], v[46:47] op_sel_hi:[0,1,1]
	v_pk_mul_f32 v[72:73], v[72:73], v[76:77]
	v_pk_fma_f32 v[8:9], v[18:19], v[8:9], v[150:151] op_sel_hi:[0,1,1]
	v_med3_f32 v6, v6, s81, v170
	v_med3_f32 v7, v7, s81, v170
	v_cvt_pk_fp8_f32 v68, v72, v73 op_sel:[0,0,1]
	v_pk_mul_f32 v[2:3], v[2:3], v[6:7]
	v_med3_f32 v6, v8, s81, v170
	v_med3_f32 v7, v9, s81, v170
	v_pk_add_f32 v[188:189], v[188:189], 1.0 op_sel_hi:[1,0]
	v_cvt_pk_fp8_f32 v54, v52, v53 op_sel:[0,0,1]
	v_mov_b32_e32 v30, v143
	v_pk_mul_f32 v[184:185], v[14:15], v[188:189]
	v_rcp_f32_e32 v184, v184
	v_rcp_f32_e32 v185, v185
	s_nop 0
	v_pk_mul_f32 v[186:187], v[184:185], v[188:189]
	v_pk_mul_f32 v[188:189], v[184:185], v[14:15]
	v_pk_mul_f32 v[2:3], v[2:3], v[186:187]
	v_cvt_pk_fp8_f32 v30, v26, v27
	v_mov_b32_e32 v14, v143
	v_mov_b32_e32 v15, v143
	v_cvt_pk_fp8_f32 v14, v10, v11
	v_cvt_pk_fp8_f32 v15, v2, v3
	ds_write_b64 v108, v[68:69]
	ds_write_b64 v108, v[54:55] offset:768
	v_add_u32_e32 v38, 0x80, v106
	ds_read_b128 v[34:37], v109
	v_ashrrev_i32_e32 v39, 31, v38
	v_pk_mul_f32 v[2:3], v[4:5], v[188:189]
	v_lshl_add_u32 v38, v38, 10, v142
	v_cvt_pk_fp8_f32 v30, v28, v29 op_sel:[0,0,1]
	v_pk_mul_f32 v[2:3], v[2:3], v[6:7]
	v_cvt_pk_fp8_f32 v14, v12, v13 op_sel:[0,0,1]
	v_cvt_pk_fp8_f32 v15, v2, v3 op_sel:[0,0,1]
	s_add_u32 s86, s18, s10
	s_addc_u32 s87, s19, s11
	v_mov_b32_e32 v2, v38
	s_waitcnt lgkmcnt(0)
	global_store_dwordx4 v2, v[34:37], s[86:87]
	ds_write_b64 v108, v[30:31]
	ds_write_b64 v108, v[14:15] offset:768
	v_add_u32_e32 v6, 0xa0, v106
	ds_read_b128 v[2:5], v109
	v_ashrrev_i32_e32 v7, 31, v6
	v_lshl_add_u32 v6, v6, 10, v142
	s_add_u32 s86, s18, s10
	s_addc_u32 s87, s19, s11
	s_and_b64 vcc, exec, s[8:9]
	s_mov_b64 s[8:9], -1
	s_waitcnt lgkmcnt(0)
	global_store_dwordx4 v6, v[2:5], s[86:87]
	s_cbranch_vccnz .LBB0_3339
	s_lshl_b64 s[8:9], s[70:71], 12
	s_add_u32 s11, s6, s8
	s_addc_u32 s65, s7, s9
	s_lshl_b32 s8, s64, 7
	s_ashr_i32 s9, s8, 31
	v_mov_b32_e32 v2, v0
	s_lshl_b64 s[8:9], s[8:9], 1
	s_add_u32 s8, s11, s8
	v_readfirstlane_b32 s10, v2
	s_addc_u32 s9, s65, s9
	s_and_b32 s11, s10, 0xc0
	s_add_u32 s8, s8, s11
	s_addc_u32 s9, s9, 0
	v_and_b32_e32 v3, 48, v2
	global_load_dwordx4 v[46:49], v3, s[8:9]
	global_load_dwordx4 v[42:45], v3, s[8:9] offset:2048
	s_ashr_i32 s9, s10, 2
	s_lshl_b32 s8, s66, 8
	s_andn2_b32 s9, s9, 63
	s_add_i32 s9, s9, s8
	v_and_or_b32 v2, v2, 15, s9
	v_lshlrev_b32_e32 v4, 2, v2
	global_load_dword v179, v4, s[14:15] offset:0
	global_load_dword v178, v4, s[14:15] offset:64
	global_load_dword v177, v4, s[14:15] offset:128
	global_load_dword v176, v4, s[14:15] offset:192
	global_load_dword v175, v4, s[14:15] offset:512
	global_load_dword v174, v4, s[14:15] offset:576
	global_load_dword v171, v4, s[14:15] offset:640
	global_load_dword v169, v4, s[14:15] offset:704
	s_andn2_b64 vcc, exec, s[16:17]
	s_cbranch_vccnz .LBB0_3338
	s_barrier
	s_branch .LBB0_3338
